# stack7 + cooperative L2 touch of the expert weight tile (B operand) in the MoE up-projection
# baseline (speedup 1.0000x reference)
; template <class Epi, class Sched>
; __device__ __forceinline__ void gemm_phase(LAS unsigned char* lds, const Sched& S, const Epi& E, const int wid) {
;     ...
;         for (int t = 0; t < nt; t += 2) {
;             const bool last = (t == nt - 2);
;             const char* a1 = cA + (size_t)(t + 1) * kstep;
;             const char* a2 = last ? nA : cA + (size_t)(t + 2) * kstep; const char* b2 = last ? nB : cB + (size_t)(t + 2) * kstep;
;             const char* a3 = a2 + kstep; const char* b3 = b2 + kstep;
.LBB7_779:
	s_cmp_gt_u32 s94, 1
	s_cbranch_scc1 .Lp5_notouch
	s_sub_i32 s99, s78, 2
	s_lshl_b32 s99, s99, 7
	s_cmp_gt_i32 s78, 0
	s_cselect_b32 s100, s75, s76
	s_cselect_b32 s101, s39, s77
	s_cselect_b32 s99, s99, 0x100
	s_add_u32 s100, s100, s99
	s_addc_u32 s101, s101, 0
	s_lshl_b32 s99, s94, 7
	s_add_u32 s100, s100, s99
	s_addc_u32 s101, s101, 0
	s_lshr_b32 s99, s95, 3
	s_and_b32 s99, s99, 3
	s_lshl_b32 s99, s99, 6
	v_mbcnt_lo_u32_b32 v149, -1, 0
	v_mbcnt_hi_u32_b32 v149, -1, v149
	v_add_u32_e32 v149, s99, v149
	v_lshlrev_b32_e32 v149, 10, v149
	global_load_dword v149, v149, s[100:101]
